# merge GEMM epilogue: nt hint on the read-once fp8 merge-gate loads
# speedup vs baseline: 1.0067x; 1.0067x over previous
; __device__ __forceinline__ float frcp_(float x) { return __builtin_amdgcn_rcpf(x); }
;     template <bool HI> static __device__ __forceinline__ f32x2 e1p(unsigned w) { const auto x = __builtin_amdgcn_cvt_pk_f32_fp8((int)w, HI); f32x2 e; e.x = __builtin_amdgcn_exp2f(x[0]); e.y = __builtin_amdgcn_exp2f(x[1]); return e + 1.0f; }
;     static __device__ __forceinline__ f32x2 rcp2(f32x2 d) { f32x2 r; r.x = frcp_(d.x); r.y = frcp_(d.y); return r; }
.LBB0_664:
	s_and_b32 s6, s76, 0xffff
	s_lshl_b32 s33, s77, 3
	s_add_i32 s33, s6, s33
	s_add_i32 s34, s33, 4
	s_ashr_i32 s35, s34, 31
	s_lshl_b64 s[34:35], s[34:35], 16
	v_lshl_add_u64 v[134:135], v[204:205], 0, s[34:35]
	global_load_dwordx4 v[164:167], v[134:135], off nt
	global_load_dwordx4 v[158:161], v[134:135], off offset:1024 nt
	global_load_dwordx4 v[154:157], v[134:135], off offset:2048 nt
	global_load_dwordx4 v[150:153], v[134:135], off offset:3072 nt
	v_lshl_add_u32 v4, s77, 8, v212
	v_ashrrev_i32_e32 v5, 31, v4
	v_or_b32_e32 v136, 16, v4
	v_lshlrev_b64 v[138:139], 11, v[4:5]
	v_add_co_u32_e32 v134, vcc, 0x1000, v134
	v_lshl_or_b32 v2, s6, 9, v215
	v_ashrrev_i32_e32 v137, 31, v136
	v_lshl_add_u64 v[138:139], s[10:11], 0, v[138:139]
	v_addc_co_u32_e32 v135, vcc, 0, v135, vcc
	v_lshlrev_b64 v[168:169], 11, v[136:137]
	v_lshl_add_u64 v[162:163], v[138:139], 0, v[2:3]
	global_load_dwordx4 v[146:149], v[134:135], off nt
	global_load_dwordx4 v[142:145], v[134:135], off offset:1024 nt
	global_load_dwordx4 v[138:141], v[134:135], off offset:2048 nt
	s_nop 0
	global_load_dwordx4 v[134:137], v[134:135], off offset:3072 nt
	v_lshl_add_u64 v[168:169], s[10:11], 0, v[168:169]
	v_lshl_add_u64 v[168:169], v[168:169], 0, v[2:3]
	s_waitcnt vmcnt(0)
	v_cvt_pk_f32_fp8_e32 v[170:171], v164
	v_cvt_pk_f32_fp8_sdwa v[172:173], v164 src0_sel:WORD_1
	v_cvt_pk_f32_fp8_e32 v[174:175], v165
	v_cvt_pk_f32_fp8_sdwa v[164:165], v165 src0_sel:WORD_1
	v_cvt_pk_f32_fp8_e32 v[176:177], v166
	v_cvt_pk_f32_fp8_sdwa v[178:179], v166 src0_sel:WORD_1
	v_cvt_pk_f32_fp8_e32 v[180:181], v167
	v_cvt_pk_f32_fp8_sdwa v[166:167], v167 src0_sel:WORD_1
	v_exp_f32_e32 v170, v170
	v_exp_f32_e32 v171, v171
	v_exp_f32_e32 v172, v172
	v_exp_f32_e32 v173, v173
	v_exp_f32_e32 v174, v174
	v_exp_f32_e32 v175, v175
	v_exp_f32_e32 v164, v164
	v_exp_f32_e32 v165, v165
	v_exp_f32_e32 v166, v166
	v_exp_f32_e32 v167, v167
	v_pk_add_f32 v[170:171], v[170:171], 1.0 op_sel_hi:[1,0]
	v_pk_add_f32 v[172:173], v[172:173], 1.0 op_sel_hi:[1,0]
	v_pk_add_f32 v[174:175], v[174:175], 1.0 op_sel_hi:[1,0]
	v_pk_add_f32 v[164:165], v[164:165], 1.0 op_sel_hi:[1,0]
	v_rcp_f32_e32 v170, v170
	v_rcp_f32_e32 v171, v171
	v_rcp_f32_e32 v172, v172
	v_rcp_f32_e32 v173, v173
	v_rcp_f32_e32 v174, v174
	v_rcp_f32_e32 v175, v175
	v_rcp_f32_e32 v164, v164
	v_rcp_f32_e32 v165, v165
	v_exp_f32_e32 v176, v176
	v_exp_f32_e32 v177, v177
	v_exp_f32_e32 v178, v178
	v_exp_f32_e32 v179, v179
	v_exp_f32_e32 v180, v180
	v_exp_f32_e32 v181, v181
	v_pk_add_f32 v[166:167], v[166:167], 1.0 op_sel_hi:[1,0]
	v_cvt_pk_f32_fp8_e32 v[182:183], v158
	v_rcp_f32_e32 v188, v166
	v_rcp_f32_e32 v189, v167
	v_pk_mul_f32 v[166:167], v[114:115], v[170:171]
	v_cvt_pk_f32_fp8_sdwa v[184:185], v158 src0_sel:WORD_1
	v_pk_mul_f32 v[170:171], v[116:117], v[172:173]
	v_pk_mul_f32 v[172:173], v[110:111], v[174:175]
	v_pk_mul_f32 v[164:165], v[112:113], v[164:165]
	v_cvt_pk_bf16_f32 v5, v166, v167
	v_cvt_pk_bf16_f32 v158, v170, v171
	v_cvt_pk_bf16_f32 v166, v172, v173
	v_pk_add_f32 v[176:177], v[176:177], 1.0 op_sel_hi:[1,0]
	v_cvt_pk_bf16_f32 v167, v164, v165
	v_pk_add_f32 v[178:179], v[178:179], 1.0 op_sel_hi:[1,0]
	v_pk_add_f32 v[180:181], v[180:181], 1.0 op_sel_hi:[1,0]
	ds_bpermute_b32 v164, v213, v5
	ds_bpermute_b32 v165, v213, v158
	ds_bpermute_b32 v166, v213, v166
	ds_bpermute_b32 v167, v213, v167
	v_rcp_f32_e32 v176, v176
	v_rcp_f32_e32 v177, v177
	v_rcp_f32_e32 v178, v178
	v_rcp_f32_e32 v179, v179
	v_rcp_f32_e32 v180, v180
	v_rcp_f32_e32 v181, v181
	v_pk_mul_f32 v[170:171], v[66:67], v[176:177]
	v_pk_mul_f32 v[172:173], v[68:69], v[178:179]
	v_pk_mul_f32 v[176:177], v[64:65], v[188:189]
	v_pk_mul_f32 v[174:175], v[62:63], v[180:181]
	s_waitcnt lgkmcnt(0)
	global_store_dwordx4 v[162:163], v[164:167], off
	v_cvt_pk_bf16_f32 v5, v170, v171
	v_cvt_pk_bf16_f32 v158, v172, v173
	ds_bpermute_b32 v164, v213, v5
	ds_bpermute_b32 v165, v213, v158
	v_cvt_pk_bf16_f32 v166, v174, v175
	v_cvt_pk_bf16_f32 v167, v176, v177
	ds_bpermute_b32 v166, v213, v166
	ds_bpermute_b32 v167, v213, v167
	v_cvt_pk_f32_fp8_e32 v[186:187], v159
	v_exp_f32_e32 v184, v184
	v_exp_f32_e32 v185, v185
	v_exp_f32_e32 v182, v182
	s_waitcnt lgkmcnt(0)
	global_store_dwordx4 v[162:163], v[164:167], off offset:256
	v_exp_f32_e32 v172, v186
	v_exp_f32_e32 v173, v187
	v_cvt_pk_f32_fp8_sdwa v[166:167], v159 src0_sel:WORD_1
	v_pk_add_f32 v[164:165], v[184:185], 1.0 op_sel_hi:[1,0]
	v_exp_f32_e32 v183, v183
	v_rcp_f32_e32 v158, v164
	v_rcp_f32_e32 v159, v165
	v_exp_f32_e32 v164, v166
	v_exp_f32_e32 v165, v167
	v_pk_add_f32 v[166:167], v[172:173], 1.0 op_sel_hi:[1,0]
	v_pk_add_f32 v[170:171], v[182:183], 1.0 op_sel_hi:[1,0]
	v_rcp_f32_e32 v166, v166
	v_rcp_f32_e32 v167, v167
	v_pk_add_f32 v[164:165], v[164:165], 1.0 op_sel_hi:[1,0]
	v_rcp_f32_e32 v170, v170
	v_rcp_f32_e32 v171, v171
	v_rcp_f32_e32 v164, v164
	v_rcp_f32_e32 v165, v165
	v_pk_mul_f32 v[158:159], v[104:105], v[158:159]
	v_pk_mul_f32 v[166:167], v[94:95], v[166:167]
	v_pk_mul_f32 v[170:171], v[102:103], v[170:171]
	v_pk_mul_f32 v[164:165], v[96:97], v[164:165]
	v_cvt_pk_bf16_f32 v5, v170, v171
	v_cvt_pk_bf16_f32 v158, v158, v159
	v_cvt_pk_bf16_f32 v166, v166, v167
	ds_bpermute_b32 v166, v213, v166
	v_cvt_pk_bf16_f32 v167, v164, v165
	ds_bpermute_b32 v164, v213, v5
	ds_bpermute_b32 v165, v213, v158
	ds_bpermute_b32 v167, v213, v167
	v_cvt_pk_f32_fp8_sdwa v[170:171], v160 src0_sel:WORD_1
	v_cvt_pk_f32_fp8_e32 v[158:159], v160
	s_waitcnt lgkmcnt(0)
	global_store_dwordx4 v[168:169], v[164:167], off
	s_nop 1
	v_exp_f32_e32 v164, v170
	v_exp_f32_e32 v165, v171
	v_cvt_pk_f32_fp8_e32 v[166:167], v161
	v_cvt_pk_f32_fp8_sdwa v[170:171], v161 src0_sel:WORD_1
	v_exp_f32_e32 v158, v158
	v_exp_f32_e32 v159, v159
	v_pk_add_f32 v[164:165], v[164:165], 1.0 op_sel_hi:[1,0]
	v_exp_f32_e32 v166, v166
	v_rcp_f32_e32 v160, v164
	v_exp_f32_e32 v167, v167
	v_rcp_f32_e32 v161, v165
	v_exp_f32_e32 v164, v170
	v_exp_f32_e32 v165, v171
	v_pk_add_f32 v[158:159], v[158:159], 1.0 op_sel_hi:[1,0]
	v_pk_add_f32 v[166:167], v[166:167], 1.0 op_sel_hi:[1,0]
	v_rcp_f32_e32 v158, v158
	v_rcp_f32_e32 v159, v159
	v_pk_add_f32 v[164:165], v[164:165], 1.0 op_sel_hi:[1,0]
	v_rcp_f32_e32 v166, v166
	v_rcp_f32_e32 v167, v167
	v_rcp_f32_e32 v164, v164
	v_rcp_f32_e32 v165, v165
	v_pk_mul_f32 v[158:159], v[58:59], v[158:159]
	v_pk_mul_f32 v[160:161], v[60:61], v[160:161]
	v_pk_mul_f32 v[166:167], v[54:55], v[166:167]
	v_pk_mul_f32 v[164:165], v[56:57], v[164:165]
	v_cvt_pk_bf16_f32 v5, v158, v159
	v_cvt_pk_bf16_f32 v159, v160, v161
	v_cvt_pk_bf16_f32 v160, v166, v167
	ds_bpermute_b32 v158, v213, v5
	v_cvt_pk_bf16_f32 v161, v164, v165
	ds_bpermute_b32 v159, v213, v159
	ds_bpermute_b32 v160, v213, v160
	ds_bpermute_b32 v161, v213, v161
	v_cvt_pk_f32_fp8_e32 v[164:165], v154
	s_waitcnt lgkmcnt(0)
	global_store_dwordx4 v[168:169], v[158:161], off offset:256
	s_nop 1
	v_exp_f32_e32 v160, v164
	v_exp_f32_e32 v161, v165
	v_cvt_pk_f32_fp8_sdwa v[164:165], v154 src0_sel:WORD_1
	v_or_b32_e32 v158, 32, v4
	v_ashrrev_i32_e32 v159, 31, v158
	v_lshlrev_b64 v[166:167], 11, v[158:159]
	v_pk_add_f32 v[158:159], v[160:161], 1.0 op_sel_hi:[1,0]
	v_exp_f32_e32 v160, v164
	v_exp_f32_e32 v161, v165
	v_cvt_pk_f32_fp8_e32 v[164:165], v155
	v_cvt_pk_f32_fp8_sdwa v[168:169], v155 src0_sel:WORD_1
	v_rcp_f32_e32 v158, v158
	v_pk_add_f32 v[160:161], v[160:161], 1.0 op_sel_hi:[1,0]
	v_exp_f32_e32 v164, v164
	v_rcp_f32_e32 v154, v160
	v_exp_f32_e32 v165, v165
	v_rcp_f32_e32 v155, v161
	v_exp_f32_e32 v160, v168
	v_exp_f32_e32 v161, v169
	v_pk_add_f32 v[164:165], v[164:165], 1.0 op_sel_hi:[1,0]
	v_rcp_f32_e32 v159, v159
	v_rcp_f32_e32 v164, v164
	v_pk_add_f32 v[160:161], v[160:161], 1.0 op_sel_hi:[1,0]
	v_rcp_f32_e32 v165, v165
	v_rcp_f32_e32 v160, v160
	v_rcp_f32_e32 v161, v161
	v_pk_mul_f32 v[154:155], v[88:89], v[154:155]
	v_pk_mul_f32 v[164:165], v[78:79], v[164:165]
	v_pk_mul_f32 v[158:159], v[86:87], v[158:159]
	v_pk_mul_f32 v[160:161], v[80:81], v[160:161]
	v_cvt_pk_bf16_f32 v5, v158, v159
	v_cvt_pk_bf16_f32 v154, v154, v155
	v_cvt_pk_bf16_f32 v164, v164, v165
	ds_bpermute_b32 v158, v213, v5
	v_cvt_pk_bf16_f32 v161, v160, v161
	ds_bpermute_b32 v159, v213, v154
	ds_bpermute_b32 v160, v213, v164
	ds_bpermute_b32 v161, v213, v161
	v_lshl_add_u64 v[164:165], s[10:11], 0, v[166:167]
	v_cvt_pk_f32_fp8_sdwa v[166:167], v156 src0_sel:WORD_1
	v_lshl_add_u64 v[164:165], v[164:165], 0, v[2:3]
	v_cvt_pk_f32_fp8_e32 v[154:155], v156
	s_waitcnt lgkmcnt(0)
	global_store_dwordx4 v[164:165], v[158:161], off
	v_exp_f32_e32 v154, v154
	s_nop 0
	v_exp_f32_e32 v158, v166
	v_exp_f32_e32 v159, v167
	v_cvt_pk_f32_fp8_e32 v[160:161], v157
	v_cvt_pk_f32_fp8_sdwa v[166:167], v157 src0_sel:WORD_1
	v_exp_f32_e32 v155, v155
	v_pk_add_f32 v[158:159], v[158:159], 1.0 op_sel_hi:[1,0]
	v_exp_f32_e32 v160, v160
	v_rcp_f32_e32 v156, v158
	v_exp_f32_e32 v161, v161
	v_rcp_f32_e32 v157, v159
	v_exp_f32_e32 v158, v166
	v_exp_f32_e32 v159, v167
	v_pk_add_f32 v[154:155], v[154:155], 1.0 op_sel_hi:[1,0]
	v_pk_add_f32 v[160:161], v[160:161], 1.0 op_sel_hi:[1,0]
	v_rcp_f32_e32 v154, v154
	v_rcp_f32_e32 v155, v155
	v_pk_add_f32 v[158:159], v[158:159], 1.0 op_sel_hi:[1,0]
	v_rcp_f32_e32 v160, v160
	v_rcp_f32_e32 v161, v161
	v_rcp_f32_e32 v158, v158
	v_rcp_f32_e32 v159, v159
	v_pk_mul_f32 v[154:155], v[50:51], v[154:155]
	v_pk_mul_f32 v[156:157], v[52:53], v[156:157]
	v_pk_mul_f32 v[160:161], v[46:47], v[160:161]
	v_pk_mul_f32 v[158:159], v[48:49], v[158:159]
	v_cvt_pk_bf16_f32 v5, v154, v155
	v_cvt_pk_bf16_f32 v155, v156, v157
	v_cvt_pk_bf16_f32 v156, v160, v161
	ds_bpermute_b32 v154, v213, v5
	v_cvt_pk_bf16_f32 v157, v158, v159
	ds_bpermute_b32 v155, v213, v155
	ds_bpermute_b32 v156, v213, v156
	ds_bpermute_b32 v157, v213, v157
	v_cvt_pk_f32_fp8_e32 v[158:159], v150
	s_waitcnt lgkmcnt(0)
	global_store_dwordx4 v[164:165], v[154:157], off offset:256
	s_nop 1
	v_exp_f32_e32 v156, v158
	v_exp_f32_e32 v157, v159
	v_cvt_pk_f32_fp8_sdwa v[158:159], v150 src0_sel:WORD_1
	v_or_b32_e32 v154, 48, v4
	v_ashrrev_i32_e32 v155, 31, v154
	v_lshlrev_b64 v[160:161], 11, v[154:155]
	v_pk_add_f32 v[154:155], v[156:157], 1.0 op_sel_hi:[1,0]
	v_exp_f32_e32 v156, v158
	v_exp_f32_e32 v157, v159
	v_cvt_pk_f32_fp8_e32 v[158:159], v151
	v_cvt_pk_f32_fp8_sdwa v[164:165], v151 src0_sel:WORD_1
	v_rcp_f32_e32 v154, v154
	v_pk_add_f32 v[156:157], v[156:157], 1.0 op_sel_hi:[1,0]
	v_exp_f32_e32 v158, v158
	v_rcp_f32_e32 v150, v156
	v_exp_f32_e32 v159, v159
	v_rcp_f32_e32 v151, v157
	v_exp_f32_e32 v156, v164
	v_exp_f32_e32 v157, v165
	v_pk_add_f32 v[158:159], v[158:159], 1.0 op_sel_hi:[1,0]
	v_rcp_f32_e32 v155, v155
	v_rcp_f32_e32 v158, v158
	v_pk_add_f32 v[156:157], v[156:157], 1.0 op_sel_hi:[1,0]
	v_rcp_f32_e32 v159, v159
	v_rcp_f32_e32 v156, v156
	v_rcp_f32_e32 v157, v157
	v_pk_mul_f32 v[150:151], v[76:77], v[150:151]
	v_pk_mul_f32 v[158:159], v[70:71], v[158:159]
	v_pk_mul_f32 v[154:155], v[74:75], v[154:155]
	v_pk_mul_f32 v[156:157], v[72:73], v[156:157]
	v_cvt_pk_bf16_f32 v5, v154, v155
	v_cvt_pk_bf16_f32 v150, v150, v151
	v_cvt_pk_bf16_f32 v158, v158, v159
	ds_bpermute_b32 v154, v213, v5
	v_cvt_pk_bf16_f32 v157, v156, v157
	ds_bpermute_b32 v155, v213, v150
	ds_bpermute_b32 v156, v213, v158
	ds_bpermute_b32 v157, v213, v157
	v_lshl_add_u64 v[158:159], s[10:11], 0, v[160:161]
	v_cvt_pk_f32_fp8_sdwa v[160:161], v152 src0_sel:WORD_1
	v_lshl_add_u64 v[158:159], v[158:159], 0, v[2:3]
	v_cvt_pk_f32_fp8_e32 v[150:151], v152
	s_waitcnt lgkmcnt(0)
	global_store_dwordx4 v[158:159], v[154:157], off
	v_exp_f32_e32 v150, v150
	s_nop 0
	v_exp_f32_e32 v154, v160
	v_exp_f32_e32 v155, v161
	v_cvt_pk_f32_fp8_sdwa v[160:161], v153 src0_sel:WORD_1
	v_cvt_pk_f32_fp8_e32 v[156:157], v153
	v_exp_f32_e32 v151, v151
	v_pk_add_f32 v[154:155], v[154:155], 1.0 op_sel_hi:[1,0]
	v_exp_f32_e32 v156, v156
	v_rcp_f32_e32 v152, v154
	v_rcp_f32_e32 v153, v155
	v_exp_f32_e32 v154, v160
	v_exp_f32_e32 v155, v161
	v_exp_f32_e32 v157, v157
	v_pk_add_f32 v[150:151], v[150:151], 1.0 op_sel_hi:[1,0]
	v_pk_mul_f32 v[152:153], v[44:45], v[152:153]
	v_pk_add_f32 v[154:155], v[154:155], 1.0 op_sel_hi:[1,0]
	v_rcp_f32_e32 v150, v150
	v_rcp_f32_e32 v151, v151
	v_pk_add_f32 v[156:157], v[156:157], 1.0 op_sel_hi:[1,0]
	v_rcp_f32_e32 v154, v154
	v_rcp_f32_e32 v155, v155
	v_rcp_f32_e32 v156, v156
	v_rcp_f32_e32 v157, v157
	v_pk_mul_f32 v[150:151], v[42:43], v[150:151]
	v_pk_mul_f32 v[154:155], v[40:41], v[154:155]
	v_cvt_pk_bf16_f32 v5, v150, v151
	v_pk_mul_f32 v[156:157], v[38:39], v[156:157]
	v_cvt_pk_bf16_f32 v151, v152, v153
	ds_bpermute_b32 v150, v213, v5
	v_cvt_pk_bf16_f32 v152, v156, v157
	v_cvt_pk_bf16_f32 v153, v154, v155
	v_cvt_pk_f32_fp8_e32 v[154:155], v146
	ds_bpermute_b32 v151, v213, v151
	ds_bpermute_b32 v152, v213, v152
	ds_bpermute_b32 v153, v213, v153
	v_cvt_pk_f32_fp8_sdwa v[156:157], v146 src0_sel:WORD_1
	v_exp_f32_e32 v154, v154
	v_exp_f32_e32 v155, v155
	s_waitcnt lgkmcnt(0)
	global_store_dwordx4 v[158:159], v[150:153], off offset:256
	s_nop 1
	v_exp_f32_e32 v152, v156
	v_exp_f32_e32 v153, v157
	v_pk_add_f32 v[150:151], v[154:155], 1.0 op_sel_hi:[1,0]
	v_cvt_pk_f32_fp8_e32 v[154:155], v147
	v_cvt_pk_f32_fp8_sdwa v[156:157], v147 src0_sel:WORD_1
	v_pk_add_f32 v[152:153], v[152:153], 1.0 op_sel_hi:[1,0]
	v_rcp_f32_e32 v150, v150
	v_rcp_f32_e32 v146, v152
	v_exp_f32_e32 v154, v154
	v_exp_f32_e32 v155, v155
	v_rcp_f32_e32 v147, v153
	v_exp_f32_e32 v152, v156
	v_exp_f32_e32 v153, v157
	v_pk_add_f32 v[154:155], v[154:155], 1.0 op_sel_hi:[1,0]
	v_rcp_f32_e32 v151, v151
	v_rcp_f32_e32 v154, v154
	v_pk_add_f32 v[152:153], v[152:153], 1.0 op_sel_hi:[1,0]
	v_rcp_f32_e32 v155, v155
	v_rcp_f32_e32 v152, v152
	v_rcp_f32_e32 v153, v153
	v_pk_mul_f32 v[150:151], v[34:35], v[150:151]
	v_pk_mul_f32 v[154:155], v[30:31], v[154:155]
	v_pk_mul_f32 v[146:147], v[36:37], v[146:147]
	v_pk_mul_f32 v[152:153], v[32:33], v[152:153]
	v_cvt_pk_bf16_f32 v5, v150, v151
	v_cvt_pk_bf16_f32 v151, v146, v147
	v_cvt_pk_bf16_f32 v154, v154, v155
	ds_bpermute_b32 v150, v213, v5
	v_cvt_pk_bf16_f32 v153, v152, v153
	ds_bpermute_b32 v151, v213, v151
	ds_bpermute_b32 v152, v213, v154
	ds_bpermute_b32 v153, v213, v153
	v_cvt_pk_f32_fp8_sdwa v[154:155], v148 src0_sel:WORD_1
	v_add_co_u32_e32 v156, vcc, s78, v162
	v_cvt_pk_f32_fp8_e32 v[146:147], v148
	s_nop 0
	v_addc_co_u32_e32 v157, vcc, 0, v163, vcc
	s_waitcnt lgkmcnt(0)
	global_store_dwordx4 v[156:157], v[150:153], off
	v_exp_f32_e32 v146, v146
	v_exp_f32_e32 v147, v147
	v_exp_f32_e32 v150, v154
	v_exp_f32_e32 v151, v155
	v_cvt_pk_f32_fp8_e32 v[152:153], v149
	v_cvt_pk_f32_fp8_sdwa v[154:155], v149 src0_sel:WORD_1
	v_pk_add_f32 v[146:147], v[146:147], 1.0 op_sel_hi:[1,0]
	v_pk_add_f32 v[150:151], v[150:151], 1.0 op_sel_hi:[1,0]
	v_exp_f32_e32 v152, v152
	v_rcp_f32_e32 v148, v150
	v_exp_f32_e32 v153, v153
	v_rcp_f32_e32 v149, v151
	v_exp_f32_e32 v150, v154
	v_exp_f32_e32 v151, v155
	v_rcp_f32_e32 v146, v146
	v_rcp_f32_e32 v147, v147
	v_pk_add_f32 v[152:153], v[152:153], 1.0 op_sel_hi:[1,0]
	v_pk_add_f32 v[150:151], v[150:151], 1.0 op_sel_hi:[1,0]
	v_rcp_f32_e32 v152, v152
	v_rcp_f32_e32 v153, v153
	v_rcp_f32_e32 v150, v150
	v_rcp_f32_e32 v151, v151
	v_pk_mul_f32 v[146:147], v[82:83], v[146:147]
	v_pk_mul_f32 v[148:149], v[84:85], v[148:149]
	v_pk_mul_f32 v[152:153], v[90:91], v[152:153]
	v_pk_mul_f32 v[150:151], v[92:93], v[150:151]
	v_cvt_pk_bf16_f32 v5, v146, v147
	v_cvt_pk_bf16_f32 v147, v148, v149
	v_cvt_pk_bf16_f32 v148, v152, v153
	ds_bpermute_b32 v146, v213, v5
	v_cvt_pk_bf16_f32 v149, v150, v151
	ds_bpermute_b32 v147, v213, v147
	ds_bpermute_b32 v148, v213, v148
	ds_bpermute_b32 v149, v213, v149
	v_cvt_pk_f32_fp8_e32 v[150:151], v142
	v_lshl_add_u64 v[152:153], v[162:163], 0, s[16:17]
	v_cvt_pk_f32_fp8_sdwa v[154:155], v143 src0_sel:WORD_1
	s_waitcnt lgkmcnt(0)
	global_store_dwordx4 v[152:153], v[146:149], off offset:256
	s_nop 1
	v_exp_f32_e32 v148, v150
	v_exp_f32_e32 v149, v151
	v_cvt_pk_f32_fp8_sdwa v[150:151], v142 src0_sel:WORD_1
	v_add_u32_e32 v146, 0x90, v4
	v_ashrrev_i32_e32 v147, 31, v146
	v_lshlrev_b64 v[152:153], 11, v[146:147]
	v_pk_add_f32 v[146:147], v[148:149], 1.0 op_sel_hi:[1,0]
	v_exp_f32_e32 v148, v150
	v_exp_f32_e32 v149, v151
	v_cvt_pk_f32_fp8_e32 v[150:151], v143
	v_rcp_f32_e32 v146, v146
	v_rcp_f32_e32 v147, v147
	v_pk_add_f32 v[148:149], v[148:149], 1.0 op_sel_hi:[1,0]
	v_exp_f32_e32 v150, v150
	v_rcp_f32_e32 v142, v148
	v_exp_f32_e32 v151, v151
	v_rcp_f32_e32 v143, v149
	v_exp_f32_e32 v148, v154
	v_exp_f32_e32 v149, v155
	v_pk_add_f32 v[150:151], v[150:151], 1.0 op_sel_hi:[1,0]
	v_pk_mul_f32 v[142:143], v[28:29], v[142:143]
	v_rcp_f32_e32 v150, v150
	v_pk_add_f32 v[148:149], v[148:149], 1.0 op_sel_hi:[1,0]
	v_rcp_f32_e32 v151, v151
	v_rcp_f32_e32 v148, v148
	v_rcp_f32_e32 v149, v149
	v_pk_mul_f32 v[146:147], v[26:27], v[146:147]
	v_pk_mul_f32 v[150:151], v[22:23], v[150:151]
	v_cvt_pk_bf16_f32 v5, v146, v147
	v_pk_mul_f32 v[148:149], v[24:25], v[148:149]
	v_cvt_pk_bf16_f32 v142, v142, v143
	v_cvt_pk_bf16_f32 v150, v150, v151
	ds_bpermute_b32 v146, v213, v5
	v_cvt_pk_bf16_f32 v149, v148, v149
	ds_bpermute_b32 v147, v213, v142
	ds_bpermute_b32 v148, v213, v150
	ds_bpermute_b32 v149, v213, v149
	v_lshl_add_u64 v[150:151], s[10:11], 0, v[152:153]
	v_cvt_pk_f32_fp8_sdwa v[152:153], v144 src0_sel:WORD_1
	v_lshl_add_u64 v[150:151], v[150:151], 0, v[2:3]
	v_cvt_pk_f32_fp8_e32 v[142:143], v144
	s_waitcnt lgkmcnt(0)
	global_store_dwordx4 v[150:151], v[146:149], off
	v_exp_f32_e32 v142, v142
	s_nop 0
	v_exp_f32_e32 v146, v152
	v_exp_f32_e32 v147, v153
	v_cvt_pk_f32_fp8_e32 v[148:149], v145
	v_cvt_pk_f32_fp8_sdwa v[152:153], v145 src0_sel:WORD_1
	v_exp_f32_e32 v143, v143
	v_pk_add_f32 v[146:147], v[146:147], 1.0 op_sel_hi:[1,0]
	v_exp_f32_e32 v148, v148
	v_rcp_f32_e32 v144, v146
	v_exp_f32_e32 v149, v149
	v_rcp_f32_e32 v145, v147
	v_exp_f32_e32 v146, v152
	v_exp_f32_e32 v147, v153
	v_pk_add_f32 v[142:143], v[142:143], 1.0 op_sel_hi:[1,0]
	v_pk_add_f32 v[148:149], v[148:149], 1.0 op_sel_hi:[1,0]
	v_rcp_f32_e32 v142, v142
	v_rcp_f32_e32 v143, v143
	v_pk_add_f32 v[146:147], v[146:147], 1.0 op_sel_hi:[1,0]
	v_rcp_f32_e32 v148, v148
	v_rcp_f32_e32 v149, v149
	v_rcp_f32_e32 v146, v146
	v_rcp_f32_e32 v147, v147
	v_pk_mul_f32 v[142:143], v[98:99], v[142:143]
	v_pk_mul_f32 v[144:145], v[100:101], v[144:145]
	v_pk_mul_f32 v[148:149], v[106:107], v[148:149]
	v_pk_mul_f32 v[146:147], v[108:109], v[146:147]
	v_cvt_pk_bf16_f32 v5, v142, v143
	v_cvt_pk_bf16_f32 v143, v144, v145
	v_cvt_pk_bf16_f32 v144, v148, v149
	ds_bpermute_b32 v142, v213, v5
	v_cvt_pk_bf16_f32 v145, v146, v147
	ds_bpermute_b32 v143, v213, v143
	ds_bpermute_b32 v144, v213, v144
	ds_bpermute_b32 v145, v213, v145
	v_cvt_pk_f32_fp8_e32 v[146:147], v138
	s_waitcnt lgkmcnt(0)
	global_store_dwordx4 v[150:151], v[142:145], off offset:256
	s_nop 1
	v_exp_f32_e32 v144, v146
	v_exp_f32_e32 v145, v147
	v_cvt_pk_f32_fp8_sdwa v[146:147], v138 src0_sel:WORD_1
	v_add_u32_e32 v142, 0xa0, v4
	v_ashrrev_i32_e32 v143, 31, v142
	v_lshlrev_b64 v[148:149], 11, v[142:143]
	v_pk_add_f32 v[142:143], v[144:145], 1.0 op_sel_hi:[1,0]
	v_exp_f32_e32 v144, v146
	v_exp_f32_e32 v145, v147
	v_cvt_pk_f32_fp8_e32 v[146:147], v139
	v_cvt_pk_f32_fp8_sdwa v[150:151], v139 src0_sel:WORD_1
	v_rcp_f32_e32 v142, v142
	v_pk_add_f32 v[144:145], v[144:145], 1.0 op_sel_hi:[1,0]
	v_exp_f32_e32 v146, v146
	v_rcp_f32_e32 v138, v144
	v_exp_f32_e32 v147, v147
	v_rcp_f32_e32 v139, v145
	v_exp_f32_e32 v144, v150
	v_exp_f32_e32 v145, v151
	v_pk_add_f32 v[146:147], v[146:147], 1.0 op_sel_hi:[1,0]
	v_rcp_f32_e32 v143, v143
	v_rcp_f32_e32 v146, v146
	v_pk_add_f32 v[144:145], v[144:145], 1.0 op_sel_hi:[1,0]
	v_rcp_f32_e32 v147, v147
	v_rcp_f32_e32 v144, v144
	v_rcp_f32_e32 v145, v145
	v_pk_mul_f32 v[138:139], v[20:21], v[138:139]
	v_pk_mul_f32 v[146:147], v[14:15], v[146:147]
	v_pk_mul_f32 v[142:143], v[18:19], v[142:143]
	v_pk_mul_f32 v[144:145], v[16:17], v[144:145]
	v_cvt_pk_bf16_f32 v5, v142, v143
	v_cvt_pk_bf16_f32 v138, v138, v139
	v_cvt_pk_bf16_f32 v146, v146, v147
	ds_bpermute_b32 v142, v213, v5
	v_cvt_pk_bf16_f32 v145, v144, v145
	ds_bpermute_b32 v143, v213, v138
	ds_bpermute_b32 v144, v213, v146
	ds_bpermute_b32 v145, v213, v145
	v_lshl_add_u64 v[146:147], s[10:11], 0, v[148:149]
	v_cvt_pk_f32_fp8_sdwa v[148:149], v140 src0_sel:WORD_1
	v_lshl_add_u64 v[146:147], v[146:147], 0, v[2:3]
	v_cvt_pk_f32_fp8_e32 v[138:139], v140
	s_waitcnt lgkmcnt(0)
	global_store_dwordx4 v[146:147], v[142:145], off
	v_add_u32_e32 v4, 0xb0, v4
	v_exp_f32_e32 v138, v138
	v_exp_f32_e32 v142, v148
	v_exp_f32_e32 v143, v149
	v_cvt_pk_f32_fp8_e32 v[144:145], v141
	v_cvt_pk_f32_fp8_sdwa v[148:149], v141 src0_sel:WORD_1
	v_exp_f32_e32 v139, v139
	v_pk_add_f32 v[142:143], v[142:143], 1.0 op_sel_hi:[1,0]
	v_exp_f32_e32 v144, v144
	v_rcp_f32_e32 v140, v142
	v_exp_f32_e32 v145, v145
	v_rcp_f32_e32 v141, v143
	v_exp_f32_e32 v142, v148
	v_exp_f32_e32 v143, v149
	v_pk_add_f32 v[138:139], v[138:139], 1.0 op_sel_hi:[1,0]
	v_pk_add_f32 v[144:145], v[144:145], 1.0 op_sel_hi:[1,0]
	v_rcp_f32_e32 v138, v138
	v_rcp_f32_e32 v139, v139
	v_pk_add_f32 v[142:143], v[142:143], 1.0 op_sel_hi:[1,0]
	v_rcp_f32_e32 v144, v144
	v_rcp_f32_e32 v145, v145
	v_rcp_f32_e32 v142, v142
	v_rcp_f32_e32 v143, v143
	v_pk_mul_f32 v[138:139], v[118:119], v[138:139]
	v_pk_mul_f32 v[140:141], v[120:121], v[140:141]
	v_pk_mul_f32 v[144:145], v[122:123], v[144:145]
	v_pk_mul_f32 v[142:143], v[124:125], v[142:143]
	v_cvt_pk_bf16_f32 v5, v138, v139
	v_cvt_pk_bf16_f32 v139, v140, v141
	v_cvt_pk_bf16_f32 v140, v144, v145
	ds_bpermute_b32 v138, v213, v5
	v_cvt_pk_bf16_f32 v141, v142, v143
	ds_bpermute_b32 v139, v213, v139
	ds_bpermute_b32 v140, v213, v140
	ds_bpermute_b32 v141, v213, v141
	v_cvt_pk_f32_fp8_e32 v[142:143], v134
	v_cvt_pk_f32_fp8_sdwa v[144:145], v135 src0_sel:WORD_1
	v_ashrrev_i32_e32 v5, 31, v4
	v_lshlrev_b64 v[4:5], 11, v[4:5]
	s_waitcnt lgkmcnt(0)
	global_store_dwordx4 v[146:147], v[138:141], off offset:256
	v_lshl_add_u64 v[4:5], s[10:11], 0, v[4:5]
	v_lshl_add_u64 v[4:5], v[4:5], 0, v[2:3]
	v_cvt_pk_f32_fp8_sdwa v[140:141], v134 src0_sel:WORD_1
	v_exp_f32_e32 v138, v142
	v_exp_f32_e32 v139, v143
	v_cvt_pk_f32_fp8_e32 v[142:143], v135
	v_exp_f32_e32 v140, v140
	v_exp_f32_e32 v141, v141
	v_pk_add_f32 v[138:139], v[138:139], 1.0 op_sel_hi:[1,0]
	v_exp_f32_e32 v142, v142
	v_exp_f32_e32 v143, v143
	v_pk_add_f32 v[140:141], v[140:141], 1.0 op_sel_hi:[1,0]
	v_rcp_f32_e32 v138, v138
	v_rcp_f32_e32 v134, v140
	v_rcp_f32_e32 v135, v141
	v_exp_f32_e32 v140, v144
	v_exp_f32_e32 v141, v145
	v_pk_add_f32 v[142:143], v[142:143], 1.0 op_sel_hi:[1,0]
	v_rcp_f32_e32 v139, v139
	v_rcp_f32_e32 v142, v142
	v_pk_add_f32 v[140:141], v[140:141], 1.0 op_sel_hi:[1,0]
	v_rcp_f32_e32 v143, v143
	v_rcp_f32_e32 v140, v140
	v_rcp_f32_e32 v141, v141
	v_pk_mul_f32 v[138:139], v[10:11], v[138:139]
	v_pk_mul_f32 v[134:135], v[12:13], v[134:135]
	v_pk_mul_f32 v[142:143], v[6:7], v[142:143]
	v_pk_mul_f32 v[140:141], v[8:9], v[140:141]
	v_cvt_pk_bf16_f32 v138, v138, v139
	v_cvt_pk_bf16_f32 v134, v134, v135
	v_cvt_pk_bf16_f32 v142, v142, v143
	ds_bpermute_b32 v138, v213, v138
	v_cvt_pk_bf16_f32 v141, v140, v141
	ds_bpermute_b32 v139, v213, v134
	ds_bpermute_b32 v140, v213, v142
	ds_bpermute_b32 v141, v213, v141
	v_cvt_pk_f32_fp8_sdwa v[142:143], v136 src0_sel:WORD_1
	v_cvt_pk_f32_fp8_e32 v[134:135], v136
	s_waitcnt lgkmcnt(0)
	global_store_dwordx4 v[4:5], v[138:141], off
	s_nop 1
	v_exp_f32_e32 v138, v142
	v_exp_f32_e32 v139, v143
	v_cvt_pk_f32_fp8_e32 v[140:141], v137
	v_cvt_pk_f32_fp8_sdwa v[142:143], v137 src0_sel:WORD_1
	v_exp_f32_e32 v134, v134
	v_exp_f32_e32 v135, v135
	v_pk_add_f32 v[138:139], v[138:139], 1.0 op_sel_hi:[1,0]
	v_exp_f32_e32 v140, v140
	v_rcp_f32_e32 v136, v138
	v_exp_f32_e32 v141, v141
	v_rcp_f32_e32 v137, v139
	v_exp_f32_e32 v138, v142
	v_exp_f32_e32 v139, v143
	v_pk_add_f32 v[134:135], v[134:135], 1.0 op_sel_hi:[1,0]
	v_pk_add_f32 v[140:141], v[140:141], 1.0 op_sel_hi:[1,0]
	v_rcp_f32_e32 v134, v134
	v_rcp_f32_e32 v135, v135
	v_pk_add_f32 v[138:139], v[138:139], 1.0 op_sel_hi:[1,0]
	v_rcp_f32_e32 v140, v140
	v_rcp_f32_e32 v141, v141
	v_rcp_f32_e32 v138, v138
	v_rcp_f32_e32 v139, v139
	v_pk_mul_f32 v[134:135], v[126:127], v[134:135]
	v_pk_mul_f32 v[136:137], v[128:129], v[136:137]
	v_pk_mul_f32 v[140:141], v[130:131], v[140:141]
	v_pk_mul_f32 v[138:139], v[132:133], v[138:139]
	v_cvt_pk_bf16_f32 v2, v134, v135
	v_cvt_pk_bf16_f32 v135, v136, v137
	v_cvt_pk_bf16_f32 v136, v140, v141
	ds_bpermute_b32 v134, v213, v2
	v_cvt_pk_bf16_f32 v137, v138, v139
	ds_bpermute_b32 v135, v213, v135
	ds_bpermute_b32 v136, v213, v136
	ds_bpermute_b32 v137, v213, v137
	s_waitcnt lgkmcnt(0)
	global_store_dwordx4 v[4:5], v[134:137], off offset:256
	s_cbranch_execnz .LBB0_663
.LBB0_665:
	s_lshl_b32 s6, s77, 3
	s_add_i32 s34, s6, s76
	s_ashr_i32 s35, s34, 31
	s_lshl_b64 s[40:41], s[34:35], 16
	v_lshl_add_u64 v[4:5], v[204:205], 0, s[40:41]
	global_load_dwordx4 v[190:193], v[4:5], off nt
	s_add_i32 s34, s34, 4
	s_ashr_i32 s35, s34, 31
	s_lshl_b64 s[34:35], s[34:35], 16
	v_lshl_add_u64 v[134:135], v[204:205], 0, s[34:35]
	global_load_dwordx4 v[194:197], v[134:135], off nt
	global_load_dwordx4 v[182:185], v[4:5], off offset:1024 nt
	global_load_dwordx4 v[174:177], v[4:5], off offset:2048 nt
	global_load_dwordx4 v[166:169], v[4:5], off offset:3072 nt
	global_load_dwordx4 v[186:189], v[134:135], off offset:1024 nt
	global_load_dwordx4 v[178:181], v[134:135], off offset:2048 nt
	global_load_dwordx4 v[170:173], v[134:135], off offset:3072 nt
	v_add_co_u32_e32 v4, vcc, s67, v4
	s_waitcnt vmcnt(0)
	v_cvt_pk_f32_fp8_sdwa v[220:221], v190 src0_sel:WORD_1
	v_addc_co_u32_e32 v5, vcc, 0, v5, vcc
	v_add_co_u32_e32 v138, vcc, s67, v134
	v_cvt_pk_f32_fp8_e32 v[222:223], v191
	s_nop 0
	v_addc_co_u32_e32 v139, vcc, 0, v135, vcc
	global_load_dwordx4 v[158:161], v[4:5], off nt
	global_load_dwordx4 v[150:153], v[4:5], off offset:1024 nt
	global_load_dwordx4 v[142:145], v[4:5], off offset:2048 nt
	global_load_dwordx4 v[134:137], v[4:5], off offset:3072 nt
	global_load_dwordx4 v[162:165], v[138:139], off nt
	global_load_dwordx4 v[154:157], v[138:139], off offset:1024 nt
	global_load_dwordx4 v[146:149], v[138:139], off offset:2048 nt
	s_nop 0
	global_load_dwordx4 v[138:141], v[138:139], off offset:3072 nt
	v_cvt_pk_f32_fp8_e32 v[4:5], v190
	v_cvt_pk_f32_fp8_sdwa v[190:191], v191 src0_sel:WORD_1
	v_cvt_pk_f32_fp8_e32 v[224:225], v192
	v_cvt_pk_f32_fp8_sdwa v[226:227], v192 src0_sel:WORD_1
	v_cvt_pk_f32_fp8_e32 v[228:229], v194
	v_cvt_pk_f32_fp8_sdwa v[230:231], v194 src0_sel:WORD_1
	v_cvt_pk_f32_fp8_e32 v[232:233], v195
	v_cvt_pk_f32_fp8_sdwa v[194:195], v195 src0_sel:WORD_1
	v_exp_f32_e32 v190, v190
	v_exp_f32_e32 v191, v191
	v_exp_f32_e32 v4, v4
	v_exp_f32_e32 v5, v5
	v_cvt_pk_f32_fp8_e32 v[234:235], v196
	v_cvt_pk_f32_fp8_sdwa v[236:237], v196 src0_sel:WORD_1
	v_exp_f32_e32 v224, v224
	v_exp_f32_e32 v225, v225
	v_exp_f32_e32 v226, v226
	v_exp_f32_e32 v227, v227
	v_exp_f32_e32 v194, v194
	v_exp_f32_e32 v195, v195
	v_pk_add_f32 v[190:191], v[190:191], 1.0 op_sel_hi:[1,0]
	v_exp_f32_e32 v228, v228
	v_exp_f32_e32 v229, v229
	v_pk_add_f32 v[4:5], v[4:5], 1.0 op_sel_hi:[1,0]
	v_rcp_f32_e32 v190, v190
	v_rcp_f32_e32 v191, v191
	v_rcp_f32_e32 v4, v4
	v_rcp_f32_e32 v5, v5
	v_exp_f32_e32 v234, v234
	v_exp_f32_e32 v235, v235
	v_exp_f32_e32 v236, v236
	v_exp_f32_e32 v237, v237
	v_pk_add_f32 v[224:225], v[224:225], 1.0 op_sel_hi:[1,0]
	v_pk_add_f32 v[226:227], v[226:227], 1.0 op_sel_hi:[1,0]
	v_pk_add_f32 v[194:195], v[194:195], 1.0 op_sel_hi:[1,0]
	v_rcp_f32_e32 v224, v224
	v_rcp_f32_e32 v225, v225
	v_rcp_f32_e32 v226, v226
	v_rcp_f32_e32 v227, v227
	v_pk_add_f32 v[228:229], v[228:229], 1.0 op_sel_hi:[1,0]
	v_pk_mul_f32 v[190:191], v[194:195], v[190:191]
	v_cvt_pk_f32_fp8_e32 v[194:195], v193
	v_cvt_pk_f32_fp8_sdwa v[192:193], v193 src0_sel:WORD_1
	v_pk_mul_f32 v[4:5], v[228:229], v[4:5]
	v_pk_add_f32 v[236:237], v[236:237], 1.0 op_sel_hi:[1,0]
	v_pk_mul_f32 v[114:115], v[114:115], v[4:5]
	v_pk_add_f32 v[4:5], v[234:235], 1.0 op_sel_hi:[1,0]
	v_pk_mul_f32 v[112:113], v[112:113], v[190:191]
	v_pk_mul_f32 v[4:5], v[4:5], v[224:225]
	v_pk_mul_f32 v[190:191], v[236:237], v[226:227]
	v_pk_mul_f32 v[66:67], v[66:67], v[4:5]
	v_pk_mul_f32 v[68:69], v[68:69], v[190:191]
	v_cvt_pk_f32_fp8_e32 v[190:191], v197
	v_exp_f32_e32 v4, v194
	v_exp_f32_e32 v5, v195
	v_cvt_pk_f32_fp8_sdwa v[194:195], v197 src0_sel:WORD_1
	v_exp_f32_e32 v192, v192
	v_exp_f32_e32 v193, v193
	v_exp_f32_e32 v190, v190
	v_exp_f32_e32 v191, v191
	v_pk_add_f32 v[4:5], v[4:5], 1.0 op_sel_hi:[1,0]
	v_exp_f32_e32 v194, v194
	v_exp_f32_e32 v195, v195
	v_pk_add_f32 v[192:193], v[192:193], 1.0 op_sel_hi:[1,0]
	v_rcp_f32_e32 v4, v4
	v_rcp_f32_e32 v5, v5
	v_rcp_f32_e32 v192, v192
	v_rcp_f32_e32 v193, v193
	v_pk_add_f32 v[194:195], v[194:195], 1.0 op_sel_hi:[1,0]
	v_pk_add_f32 v[190:191], v[190:191], 1.0 op_sel_hi:[1,0]
	v_exp_f32_e32 v220, v220
	v_pk_mul_f32 v[4:5], v[190:191], v[4:5]
	v_pk_mul_f32 v[190:191], v[194:195], v[192:193]
; __device__ __forceinline__ float frcp_(float x) { return __builtin_amdgcn_rcpf(x); }
;     template <bool HI> static __device__ __forceinline__ f32x2 e1p(unsigned w) { const auto x = __builtin_amdgcn_cvt_pk_f32_fp8((int)w, HI); f32x2 e; e.x = __builtin_amdgcn_exp2f(x[0]); e.y = __builtin_amdgcn_exp2f(x[1]); return e + 1.0f; }
;     static __device__ __forceinline__ f32x2 rcp2(f32x2 d) { f32x2 r; r.x = frcp_(d.x); r.y = frcp_(d.y); return r; }
	v_cvt_pk_f32_fp8_e32 v[192:193], v182
	v_pk_mul_f32 v[62:63], v[62:63], v[4:5]
	v_pk_mul_f32 v[64:65], v[64:65], v[190:191]
	v_cvt_pk_f32_fp8_e32 v[190:191], v186
	v_exp_f32_e32 v4, v192
	v_exp_f32_e32 v5, v193
	v_cvt_pk_f32_fp8_sdwa v[192:193], v182 src0_sel:WORD_1
	v_cvt_pk_f32_fp8_sdwa v[194:195], v186 src0_sel:WORD_1
	v_exp_f32_e32 v190, v190
	v_exp_f32_e32 v191, v191
	v_exp_f32_e32 v192, v192
	v_exp_f32_e32 v193, v193
	v_pk_add_f32 v[4:5], v[4:5], 1.0 op_sel_hi:[1,0]
	v_exp_f32_e32 v194, v194
	v_exp_f32_e32 v195, v195
	v_pk_add_f32 v[192:193], v[192:193], 1.0 op_sel_hi:[1,0]
	v_rcp_f32_e32 v4, v4
	v_rcp_f32_e32 v5, v5
	v_rcp_f32_e32 v192, v192
	v_rcp_f32_e32 v193, v193
	v_pk_add_f32 v[194:195], v[194:195], 1.0 op_sel_hi:[1,0]
	v_pk_add_f32 v[190:191], v[190:191], 1.0 op_sel_hi:[1,0]
	v_exp_f32_e32 v221, v221
	v_pk_mul_f32 v[4:5], v[190:191], v[4:5]
	v_pk_mul_f32 v[190:191], v[194:195], v[192:193]
	v_cvt_pk_f32_fp8_e32 v[192:193], v183
	v_cvt_pk_f32_fp8_sdwa v[182:183], v183 src0_sel:WORD_1
	v_pk_mul_f32 v[104:105], v[104:105], v[190:191]
	v_cvt_pk_f32_fp8_e32 v[190:191], v187
	v_cvt_pk_f32_fp8_sdwa v[186:187], v187 src0_sel:WORD_1
	v_exp_f32_e32 v182, v182
	v_exp_f32_e32 v183, v183
	v_pk_mul_f32 v[102:103], v[102:103], v[4:5]
	v_exp_f32_e32 v4, v192
	v_exp_f32_e32 v5, v193
	v_exp_f32_e32 v186, v186
	v_exp_f32_e32 v187, v187
	v_pk_add_f32 v[182:183], v[182:183], 1.0 op_sel_hi:[1,0]
	v_exp_f32_e32 v190, v190
	v_rcp_f32_e32 v182, v182
	v_rcp_f32_e32 v183, v183
	v_exp_f32_e32 v191, v191
	v_pk_add_f32 v[4:5], v[4:5], 1.0 op_sel_hi:[1,0]
	v_pk_add_f32 v[186:187], v[186:187], 1.0 op_sel_hi:[1,0]
	v_rcp_f32_e32 v4, v4
	v_rcp_f32_e32 v5, v5
	v_pk_mul_f32 v[182:183], v[186:187], v[182:183]
	v_cvt_pk_f32_fp8_e32 v[186:187], v184
	v_pk_add_f32 v[190:191], v[190:191], 1.0 op_sel_hi:[1,0]
	v_pk_mul_f32 v[96:97], v[96:97], v[182:183]
	v_pk_mul_f32 v[4:5], v[190:191], v[4:5]
	v_cvt_pk_f32_fp8_e32 v[182:183], v188
	v_pk_mul_f32 v[94:95], v[94:95], v[4:5]
	v_exp_f32_e32 v4, v186
	v_exp_f32_e32 v5, v187
	v_cvt_pk_f32_fp8_sdwa v[186:187], v184 src0_sel:WORD_1
	v_cvt_pk_f32_fp8_sdwa v[190:191], v188 src0_sel:WORD_1
	v_exp_f32_e32 v182, v182
	v_exp_f32_e32 v183, v183
	v_exp_f32_e32 v186, v186
	v_exp_f32_e32 v187, v187
	v_pk_add_f32 v[4:5], v[4:5], 1.0 op_sel_hi:[1,0]
	v_exp_f32_e32 v190, v190
	v_exp_f32_e32 v191, v191
	v_pk_add_f32 v[186:187], v[186:187], 1.0 op_sel_hi:[1,0]
	v_rcp_f32_e32 v4, v4
	v_rcp_f32_e32 v5, v5
	v_rcp_f32_e32 v186, v186
	v_rcp_f32_e32 v187, v187
	v_pk_add_f32 v[190:191], v[190:191], 1.0 op_sel_hi:[1,0]
	v_pk_add_f32 v[182:183], v[182:183], 1.0 op_sel_hi:[1,0]
	v_exp_f32_e32 v222, v222
	v_pk_mul_f32 v[4:5], v[182:183], v[4:5]
	v_pk_mul_f32 v[182:183], v[190:191], v[186:187]
	v_cvt_pk_f32_fp8_e32 v[186:187], v185
	v_cvt_pk_f32_fp8_sdwa v[184:185], v185 src0_sel:WORD_1
	v_pk_mul_f32 v[60:61], v[60:61], v[182:183]
	v_cvt_pk_f32_fp8_e32 v[182:183], v189
	v_pk_mul_f32 v[58:59], v[58:59], v[4:5]
	v_exp_f32_e32 v4, v186
	v_exp_f32_e32 v5, v187
	v_cvt_pk_f32_fp8_sdwa v[186:187], v189 src0_sel:WORD_1
	v_exp_f32_e32 v184, v184
	v_exp_f32_e32 v185, v185
	v_exp_f32_e32 v182, v182
	v_exp_f32_e32 v183, v183
	v_pk_add_f32 v[4:5], v[4:5], 1.0 op_sel_hi:[1,0]
	v_exp_f32_e32 v186, v186
	v_exp_f32_e32 v187, v187
	v_pk_add_f32 v[184:185], v[184:185], 1.0 op_sel_hi:[1,0]
	v_rcp_f32_e32 v4, v4
	v_rcp_f32_e32 v5, v5
	v_rcp_f32_e32 v184, v184
	v_rcp_f32_e32 v185, v185
	v_pk_add_f32 v[186:187], v[186:187], 1.0 op_sel_hi:[1,0]
	v_pk_add_f32 v[182:183], v[182:183], 1.0 op_sel_hi:[1,0]
	v_exp_f32_e32 v223, v223
	v_pk_mul_f32 v[4:5], v[182:183], v[4:5]
	v_pk_mul_f32 v[182:183], v[186:187], v[184:185]
	v_cvt_pk_f32_fp8_e32 v[184:185], v174
	v_pk_mul_f32 v[54:55], v[54:55], v[4:5]
	v_pk_mul_f32 v[56:57], v[56:57], v[182:183]
	v_cvt_pk_f32_fp8_e32 v[182:183], v178
	v_exp_f32_e32 v4, v184
	v_exp_f32_e32 v5, v185
	v_cvt_pk_f32_fp8_sdwa v[184:185], v174 src0_sel:WORD_1
	v_cvt_pk_f32_fp8_sdwa v[186:187], v178 src0_sel:WORD_1
	v_exp_f32_e32 v182, v182
	v_exp_f32_e32 v183, v183
	v_exp_f32_e32 v184, v184
	v_exp_f32_e32 v185, v185
	v_pk_add_f32 v[4:5], v[4:5], 1.0 op_sel_hi:[1,0]
	v_exp_f32_e32 v186, v186
	v_exp_f32_e32 v187, v187
	v_pk_add_f32 v[184:185], v[184:185], 1.0 op_sel_hi:[1,0]
	v_rcp_f32_e32 v4, v4
	v_rcp_f32_e32 v5, v5
	v_rcp_f32_e32 v184, v184
	v_rcp_f32_e32 v185, v185
	v_pk_add_f32 v[186:187], v[186:187], 1.0 op_sel_hi:[1,0]
	v_pk_add_f32 v[182:183], v[182:183], 1.0 op_sel_hi:[1,0]
	v_exp_f32_e32 v230, v230
	v_pk_mul_f32 v[4:5], v[182:183], v[4:5]
	v_pk_mul_f32 v[182:183], v[186:187], v[184:185]
	v_cvt_pk_f32_fp8_e32 v[184:185], v175
	v_cvt_pk_f32_fp8_sdwa v[174:175], v175 src0_sel:WORD_1
	v_pk_mul_f32 v[88:89], v[88:89], v[182:183]
	v_cvt_pk_f32_fp8_e32 v[182:183], v179
	v_cvt_pk_f32_fp8_sdwa v[178:179], v179 src0_sel:WORD_1
	v_exp_f32_e32 v174, v174
	v_exp_f32_e32 v175, v175
	v_pk_mul_f32 v[86:87], v[86:87], v[4:5]
	v_exp_f32_e32 v4, v184
	v_exp_f32_e32 v5, v185
	v_exp_f32_e32 v178, v178
	v_exp_f32_e32 v179, v179
	v_pk_add_f32 v[174:175], v[174:175], 1.0 op_sel_hi:[1,0]
	v_exp_f32_e32 v182, v182
	v_rcp_f32_e32 v174, v174
	v_rcp_f32_e32 v175, v175
	v_exp_f32_e32 v183, v183
	v_pk_add_f32 v[4:5], v[4:5], 1.0 op_sel_hi:[1,0]
	v_pk_add_f32 v[178:179], v[178:179], 1.0 op_sel_hi:[1,0]
	v_rcp_f32_e32 v4, v4
	v_rcp_f32_e32 v5, v5
	v_pk_mul_f32 v[174:175], v[178:179], v[174:175]
	v_cvt_pk_f32_fp8_e32 v[178:179], v176
	v_pk_add_f32 v[182:183], v[182:183], 1.0 op_sel_hi:[1,0]
	v_pk_mul_f32 v[80:81], v[80:81], v[174:175]
	v_pk_mul_f32 v[4:5], v[182:183], v[4:5]
	v_cvt_pk_f32_fp8_e32 v[174:175], v180
	v_pk_mul_f32 v[78:79], v[78:79], v[4:5]
	v_exp_f32_e32 v4, v178
; __device__ __forceinline__ float frcp_(float x) { return __builtin_amdgcn_rcpf(x); }
;     template <bool HI> static __device__ __forceinline__ f32x2 e1p(unsigned w) { const auto x = __builtin_amdgcn_cvt_pk_f32_fp8((int)w, HI); f32x2 e; e.x = __builtin_amdgcn_exp2f(x[0]); e.y = __builtin_amdgcn_exp2f(x[1]); return e + 1.0f; }
;     static __device__ __forceinline__ f32x2 rcp2(f32x2 d) { f32x2 r; r.x = frcp_(d.x); r.y = frcp_(d.y); return r; }
	v_exp_f32_e32 v5, v179
	v_cvt_pk_f32_fp8_sdwa v[178:179], v176 src0_sel:WORD_1
	v_cvt_pk_f32_fp8_sdwa v[182:183], v180 src0_sel:WORD_1
	v_exp_f32_e32 v174, v174
	v_exp_f32_e32 v175, v175
	v_exp_f32_e32 v178, v178
	v_exp_f32_e32 v179, v179
	v_pk_add_f32 v[4:5], v[4:5], 1.0 op_sel_hi:[1,0]
	v_exp_f32_e32 v182, v182
	v_exp_f32_e32 v183, v183
	v_pk_add_f32 v[178:179], v[178:179], 1.0 op_sel_hi:[1,0]
	v_rcp_f32_e32 v4, v4
	v_rcp_f32_e32 v5, v5
	v_rcp_f32_e32 v178, v178
	v_rcp_f32_e32 v179, v179
	v_pk_add_f32 v[182:183], v[182:183], 1.0 op_sel_hi:[1,0]
	v_pk_add_f32 v[174:175], v[174:175], 1.0 op_sel_hi:[1,0]
	v_exp_f32_e32 v231, v231
	v_pk_mul_f32 v[4:5], v[174:175], v[4:5]
	v_pk_mul_f32 v[174:175], v[182:183], v[178:179]
	v_cvt_pk_f32_fp8_e32 v[178:179], v177
	v_cvt_pk_f32_fp8_sdwa v[176:177], v177 src0_sel:WORD_1
	v_pk_mul_f32 v[52:53], v[52:53], v[174:175]
	v_cvt_pk_f32_fp8_e32 v[174:175], v181
	v_pk_mul_f32 v[50:51], v[50:51], v[4:5]
	v_exp_f32_e32 v4, v178
	v_exp_f32_e32 v5, v179
	v_cvt_pk_f32_fp8_sdwa v[178:179], v181 src0_sel:WORD_1
	v_exp_f32_e32 v176, v176
	v_exp_f32_e32 v177, v177
	v_exp_f32_e32 v174, v174
	v_exp_f32_e32 v175, v175
	v_pk_add_f32 v[4:5], v[4:5], 1.0 op_sel_hi:[1,0]
	v_exp_f32_e32 v178, v178
	v_exp_f32_e32 v179, v179
	v_pk_add_f32 v[176:177], v[176:177], 1.0 op_sel_hi:[1,0]
	v_rcp_f32_e32 v4, v4
	v_rcp_f32_e32 v5, v5
	v_rcp_f32_e32 v176, v176
	v_rcp_f32_e32 v177, v177
	v_pk_add_f32 v[178:179], v[178:179], 1.0 op_sel_hi:[1,0]
	v_pk_add_f32 v[174:175], v[174:175], 1.0 op_sel_hi:[1,0]
	v_exp_f32_e32 v232, v232
	v_pk_mul_f32 v[4:5], v[174:175], v[4:5]
	v_pk_mul_f32 v[174:175], v[178:179], v[176:177]
	v_cvt_pk_f32_fp8_e32 v[176:177], v166
	v_pk_mul_f32 v[46:47], v[46:47], v[4:5]
	v_pk_mul_f32 v[48:49], v[48:49], v[174:175]
	v_cvt_pk_f32_fp8_e32 v[174:175], v170
	v_exp_f32_e32 v4, v176
	v_exp_f32_e32 v5, v177
	v_cvt_pk_f32_fp8_sdwa v[176:177], v166 src0_sel:WORD_1
	v_cvt_pk_f32_fp8_sdwa v[178:179], v170 src0_sel:WORD_1
	v_exp_f32_e32 v174, v174
	v_exp_f32_e32 v175, v175
	v_exp_f32_e32 v176, v176
	v_exp_f32_e32 v177, v177
	v_pk_add_f32 v[4:5], v[4:5], 1.0 op_sel_hi:[1,0]
	v_exp_f32_e32 v178, v178
	v_exp_f32_e32 v179, v179
	v_pk_add_f32 v[176:177], v[176:177], 1.0 op_sel_hi:[1,0]
	v_rcp_f32_e32 v4, v4
	v_rcp_f32_e32 v5, v5
	v_rcp_f32_e32 v176, v176
	v_rcp_f32_e32 v177, v177
	v_pk_add_f32 v[178:179], v[178:179], 1.0 op_sel_hi:[1,0]
	v_pk_add_f32 v[174:175], v[174:175], 1.0 op_sel_hi:[1,0]
	v_exp_f32_e32 v233, v233
	v_pk_mul_f32 v[4:5], v[174:175], v[4:5]
	v_pk_mul_f32 v[174:175], v[178:179], v[176:177]
	v_cvt_pk_f32_fp8_e32 v[176:177], v167
	v_cvt_pk_f32_fp8_sdwa v[166:167], v167 src0_sel:WORD_1
	v_pk_mul_f32 v[76:77], v[76:77], v[174:175]
	v_cvt_pk_f32_fp8_e32 v[174:175], v171
	v_cvt_pk_f32_fp8_sdwa v[170:171], v171 src0_sel:WORD_1
	v_exp_f32_e32 v166, v166
	v_exp_f32_e32 v167, v167
	v_pk_mul_f32 v[74:75], v[74:75], v[4:5]
	v_exp_f32_e32 v4, v176
	v_exp_f32_e32 v5, v177
	v_exp_f32_e32 v170, v170
	v_exp_f32_e32 v171, v171
	v_pk_add_f32 v[166:167], v[166:167], 1.0 op_sel_hi:[1,0]
	v_exp_f32_e32 v174, v174
	v_rcp_f32_e32 v166, v166
	v_rcp_f32_e32 v167, v167
	v_exp_f32_e32 v175, v175
	v_pk_add_f32 v[4:5], v[4:5], 1.0 op_sel_hi:[1,0]
	v_pk_add_f32 v[170:171], v[170:171], 1.0 op_sel_hi:[1,0]
	v_rcp_f32_e32 v4, v4
	v_rcp_f32_e32 v5, v5
	v_pk_mul_f32 v[166:167], v[170:171], v[166:167]
	v_cvt_pk_f32_fp8_e32 v[170:171], v168
	v_pk_add_f32 v[174:175], v[174:175], 1.0 op_sel_hi:[1,0]
	v_pk_mul_f32 v[72:73], v[72:73], v[166:167]
	v_pk_mul_f32 v[4:5], v[174:175], v[4:5]
	v_cvt_pk_f32_fp8_e32 v[166:167], v172
	v_pk_mul_f32 v[70:71], v[70:71], v[4:5]
	v_exp_f32_e32 v4, v170
	v_exp_f32_e32 v5, v171
	v_cvt_pk_f32_fp8_sdwa v[170:171], v168 src0_sel:WORD_1
	v_cvt_pk_f32_fp8_sdwa v[174:175], v172 src0_sel:WORD_1
	v_exp_f32_e32 v166, v166
	v_exp_f32_e32 v167, v167
	v_exp_f32_e32 v170, v170
	v_exp_f32_e32 v171, v171
	v_pk_add_f32 v[4:5], v[4:5], 1.0 op_sel_hi:[1,0]
	v_exp_f32_e32 v174, v174
	v_exp_f32_e32 v175, v175
	v_pk_add_f32 v[170:171], v[170:171], 1.0 op_sel_hi:[1,0]
	v_rcp_f32_e32 v4, v4
	v_rcp_f32_e32 v5, v5
	v_rcp_f32_e32 v170, v170
	v_rcp_f32_e32 v171, v171
	v_pk_add_f32 v[174:175], v[174:175], 1.0 op_sel_hi:[1,0]
	v_pk_add_f32 v[166:167], v[166:167], 1.0 op_sel_hi:[1,0]
	v_pk_add_f32 v[220:221], v[220:221], 1.0 op_sel_hi:[1,0]
	v_pk_mul_f32 v[4:5], v[166:167], v[4:5]
	v_pk_mul_f32 v[166:167], v[174:175], v[170:171]
	v_cvt_pk_f32_fp8_e32 v[170:171], v169
	v_cvt_pk_f32_fp8_sdwa v[168:169], v169 src0_sel:WORD_1
	v_pk_mul_f32 v[44:45], v[44:45], v[166:167]
	v_cvt_pk_f32_fp8_e32 v[166:167], v173
	v_pk_mul_f32 v[42:43], v[42:43], v[4:5]
	v_exp_f32_e32 v4, v170
	v_exp_f32_e32 v5, v171
	v_cvt_pk_f32_fp8_sdwa v[170:171], v173 src0_sel:WORD_1
	v_exp_f32_e32 v168, v168
	v_exp_f32_e32 v169, v169
	v_exp_f32_e32 v166, v166
	v_exp_f32_e32 v167, v167
	v_pk_add_f32 v[4:5], v[4:5], 1.0 op_sel_hi:[1,0]
	v_exp_f32_e32 v170, v170
	v_exp_f32_e32 v171, v171
	v_pk_add_f32 v[168:169], v[168:169], 1.0 op_sel_hi:[1,0]
	v_rcp_f32_e32 v4, v4
	v_rcp_f32_e32 v5, v5
	v_rcp_f32_e32 v168, v168
	v_rcp_f32_e32 v169, v169
	v_pk_add_f32 v[170:171], v[170:171], 1.0 op_sel_hi:[1,0]
	v_pk_add_f32 v[166:167], v[166:167], 1.0 op_sel_hi:[1,0]
	v_pk_add_f32 v[222:223], v[222:223], 1.0 op_sel_hi:[1,0]
	v_pk_mul_f32 v[4:5], v[166:167], v[4:5]
	v_pk_mul_f32 v[166:167], v[170:171], v[168:169]
	s_waitcnt vmcnt(7)
	v_cvt_pk_f32_fp8_e32 v[168:169], v158
	v_pk_mul_f32 v[38:39], v[38:39], v[4:5]
	v_pk_mul_f32 v[40:41], v[40:41], v[166:167]
	s_waitcnt vmcnt(3)
; __device__ __forceinline__ float frcp_(float x) { return __builtin_amdgcn_rcpf(x); }
;     template <bool HI> static __device__ __forceinline__ f32x2 e1p(unsigned w) { const auto x = __builtin_amdgcn_cvt_pk_f32_fp8((int)w, HI); f32x2 e; e.x = __builtin_amdgcn_exp2f(x[0]); e.y = __builtin_amdgcn_exp2f(x[1]); return e + 1.0f; }
;     static __device__ __forceinline__ f32x2 rcp2(f32x2 d) { f32x2 r; r.x = frcp_(d.x); r.y = frcp_(d.y); return r; }
	v_cvt_pk_f32_fp8_e32 v[166:167], v162
	v_exp_f32_e32 v4, v168
	v_exp_f32_e32 v5, v169
	v_cvt_pk_f32_fp8_sdwa v[168:169], v158 src0_sel:WORD_1
	v_cvt_pk_f32_fp8_sdwa v[170:171], v162 src0_sel:WORD_1
	v_exp_f32_e32 v166, v166
	v_exp_f32_e32 v167, v167
	v_exp_f32_e32 v168, v168
	v_exp_f32_e32 v169, v169
	v_pk_add_f32 v[4:5], v[4:5], 1.0 op_sel_hi:[1,0]
	v_exp_f32_e32 v170, v170
	v_exp_f32_e32 v171, v171
	v_pk_add_f32 v[168:169], v[168:169], 1.0 op_sel_hi:[1,0]
	v_rcp_f32_e32 v4, v4
	v_rcp_f32_e32 v5, v5
	v_rcp_f32_e32 v168, v168
	v_rcp_f32_e32 v169, v169
	v_pk_add_f32 v[170:171], v[170:171], 1.0 op_sel_hi:[1,0]
	v_pk_add_f32 v[166:167], v[166:167], 1.0 op_sel_hi:[1,0]
	v_rcp_f32_e32 v220, v220
	v_pk_mul_f32 v[4:5], v[166:167], v[4:5]
	v_pk_mul_f32 v[166:167], v[170:171], v[168:169]
	v_cvt_pk_f32_fp8_e32 v[168:169], v159
	v_cvt_pk_f32_fp8_sdwa v[158:159], v159 src0_sel:WORD_1
	v_pk_mul_f32 v[36:37], v[36:37], v[166:167]
	v_cvt_pk_f32_fp8_e32 v[166:167], v163
	v_cvt_pk_f32_fp8_sdwa v[162:163], v163 src0_sel:WORD_1
	v_exp_f32_e32 v158, v158
	v_exp_f32_e32 v159, v159
	v_pk_mul_f32 v[34:35], v[34:35], v[4:5]
	v_exp_f32_e32 v4, v168
	v_exp_f32_e32 v5, v169
	v_exp_f32_e32 v162, v162
	v_exp_f32_e32 v163, v163
	v_pk_add_f32 v[158:159], v[158:159], 1.0 op_sel_hi:[1,0]
	v_exp_f32_e32 v166, v166
	v_rcp_f32_e32 v158, v158
	v_rcp_f32_e32 v159, v159
	v_exp_f32_e32 v167, v167
	v_pk_add_f32 v[4:5], v[4:5], 1.0 op_sel_hi:[1,0]
	v_pk_add_f32 v[162:163], v[162:163], 1.0 op_sel_hi:[1,0]
	v_rcp_f32_e32 v4, v4
	v_rcp_f32_e32 v5, v5
	v_pk_mul_f32 v[158:159], v[162:163], v[158:159]
	v_cvt_pk_f32_fp8_e32 v[162:163], v160
	v_pk_add_f32 v[166:167], v[166:167], 1.0 op_sel_hi:[1,0]
	v_pk_mul_f32 v[32:33], v[32:33], v[158:159]
	v_pk_mul_f32 v[4:5], v[166:167], v[4:5]
	v_cvt_pk_f32_fp8_e32 v[158:159], v164
	v_pk_mul_f32 v[30:31], v[30:31], v[4:5]
	v_exp_f32_e32 v4, v162
	v_exp_f32_e32 v5, v163
	v_cvt_pk_f32_fp8_sdwa v[162:163], v160 src0_sel:WORD_1
	v_cvt_pk_f32_fp8_sdwa v[166:167], v164 src0_sel:WORD_1
	v_exp_f32_e32 v158, v158
	v_exp_f32_e32 v159, v159
	v_exp_f32_e32 v162, v162
	v_exp_f32_e32 v163, v163
	v_pk_add_f32 v[4:5], v[4:5], 1.0 op_sel_hi:[1,0]
	v_exp_f32_e32 v166, v166
	v_exp_f32_e32 v167, v167
	v_pk_add_f32 v[162:163], v[162:163], 1.0 op_sel_hi:[1,0]
	v_rcp_f32_e32 v4, v4
	v_rcp_f32_e32 v5, v5
	v_rcp_f32_e32 v162, v162
	v_rcp_f32_e32 v163, v163
	v_pk_add_f32 v[166:167], v[166:167], 1.0 op_sel_hi:[1,0]
	v_pk_add_f32 v[158:159], v[158:159], 1.0 op_sel_hi:[1,0]
	v_rcp_f32_e32 v221, v221
	v_pk_mul_f32 v[4:5], v[158:159], v[4:5]
	v_pk_mul_f32 v[158:159], v[166:167], v[162:163]
	v_cvt_pk_f32_fp8_e32 v[162:163], v161
	v_cvt_pk_f32_fp8_sdwa v[160:161], v161 src0_sel:WORD_1
	v_pk_mul_f32 v[84:85], v[84:85], v[158:159]
	v_cvt_pk_f32_fp8_e32 v[158:159], v165
	v_pk_mul_f32 v[82:83], v[82:83], v[4:5]
	v_exp_f32_e32 v4, v162
	v_exp_f32_e32 v5, v163
	v_cvt_pk_f32_fp8_sdwa v[162:163], v165 src0_sel:WORD_1
	v_exp_f32_e32 v160, v160
	v_exp_f32_e32 v161, v161
	v_exp_f32_e32 v158, v158
	v_exp_f32_e32 v159, v159
	v_pk_add_f32 v[4:5], v[4:5], 1.0 op_sel_hi:[1,0]
	v_exp_f32_e32 v162, v162
	v_exp_f32_e32 v163, v163
	v_pk_add_f32 v[160:161], v[160:161], 1.0 op_sel_hi:[1,0]
	v_rcp_f32_e32 v4, v4
	v_rcp_f32_e32 v5, v5
	v_rcp_f32_e32 v160, v160
	v_rcp_f32_e32 v161, v161
	v_pk_add_f32 v[162:163], v[162:163], 1.0 op_sel_hi:[1,0]
	v_pk_add_f32 v[158:159], v[158:159], 1.0 op_sel_hi:[1,0]
	v_rcp_f32_e32 v222, v222
	v_pk_mul_f32 v[4:5], v[158:159], v[4:5]
	v_pk_mul_f32 v[158:159], v[162:163], v[160:161]
	v_cvt_pk_f32_fp8_e32 v[160:161], v150
	v_pk_mul_f32 v[90:91], v[90:91], v[4:5]
	v_pk_mul_f32 v[92:93], v[92:93], v[158:159]
	s_waitcnt vmcnt(2)
	v_cvt_pk_f32_fp8_e32 v[158:159], v154
	v_exp_f32_e32 v4, v160
	v_exp_f32_e32 v5, v161
	v_cvt_pk_f32_fp8_sdwa v[160:161], v150 src0_sel:WORD_1
	v_cvt_pk_f32_fp8_sdwa v[162:163], v154 src0_sel:WORD_1
	v_exp_f32_e32 v158, v158
	v_exp_f32_e32 v159, v159
	v_exp_f32_e32 v160, v160
	v_exp_f32_e32 v161, v161
	v_pk_add_f32 v[4:5], v[4:5], 1.0 op_sel_hi:[1,0]
	v_exp_f32_e32 v162, v162
	v_exp_f32_e32 v163, v163
	v_pk_add_f32 v[160:161], v[160:161], 1.0 op_sel_hi:[1,0]
	v_rcp_f32_e32 v4, v4
	v_rcp_f32_e32 v5, v5
	v_rcp_f32_e32 v160, v160
	v_rcp_f32_e32 v161, v161
	v_pk_add_f32 v[162:163], v[162:163], 1.0 op_sel_hi:[1,0]
	v_pk_add_f32 v[158:159], v[158:159], 1.0 op_sel_hi:[1,0]
	v_rcp_f32_e32 v223, v223
	v_pk_mul_f32 v[4:5], v[158:159], v[4:5]
	v_pk_mul_f32 v[158:159], v[162:163], v[160:161]
	v_cvt_pk_f32_fp8_e32 v[160:161], v151
	v_cvt_pk_f32_fp8_sdwa v[150:151], v151 src0_sel:WORD_1
	v_pk_mul_f32 v[28:29], v[28:29], v[158:159]
	v_cvt_pk_f32_fp8_e32 v[158:159], v155
	v_cvt_pk_f32_fp8_sdwa v[154:155], v155 src0_sel:WORD_1
	v_exp_f32_e32 v150, v150
	v_exp_f32_e32 v151, v151
	v_pk_mul_f32 v[26:27], v[26:27], v[4:5]
	v_exp_f32_e32 v4, v160
	v_exp_f32_e32 v5, v161
	v_exp_f32_e32 v154, v154
	v_exp_f32_e32 v155, v155
	v_pk_add_f32 v[150:151], v[150:151], 1.0 op_sel_hi:[1,0]
	v_exp_f32_e32 v158, v158
	v_rcp_f32_e32 v150, v150
	v_rcp_f32_e32 v151, v151
	v_exp_f32_e32 v159, v159
	v_pk_add_f32 v[4:5], v[4:5], 1.0 op_sel_hi:[1,0]
	v_pk_add_f32 v[154:155], v[154:155], 1.0 op_sel_hi:[1,0]
	v_rcp_f32_e32 v4, v4
	v_rcp_f32_e32 v5, v5
	v_pk_mul_f32 v[150:151], v[154:155], v[150:151]
	v_cvt_pk_f32_fp8_e32 v[154:155], v152
	v_pk_add_f32 v[158:159], v[158:159], 1.0 op_sel_hi:[1,0]
	v_pk_mul_f32 v[24:25], v[24:25], v[150:151]
	v_pk_mul_f32 v[4:5], v[158:159], v[4:5]
	v_cvt_pk_f32_fp8_e32 v[150:151], v156
	v_pk_mul_f32 v[22:23], v[22:23], v[4:5]
	v_exp_f32_e32 v4, v154
	v_exp_f32_e32 v5, v155
	v_cvt_pk_f32_fp8_sdwa v[154:155], v152 src0_sel:WORD_1
	v_cvt_pk_f32_fp8_sdwa v[158:159], v156 src0_sel:WORD_1
; __device__ __forceinline__ float frcp_(float x) { return __builtin_amdgcn_rcpf(x); }
;     template <bool HI> static __device__ __forceinline__ f32x2 e1p(unsigned w) { const auto x = __builtin_amdgcn_cvt_pk_f32_fp8((int)w, HI); f32x2 e; e.x = __builtin_amdgcn_exp2f(x[0]); e.y = __builtin_amdgcn_exp2f(x[1]); return e + 1.0f; }
;     static __device__ __forceinline__ f32x2 rcp2(f32x2 d) { f32x2 r; r.x = frcp_(d.x); r.y = frcp_(d.y); return r; }
	v_exp_f32_e32 v150, v150
	v_exp_f32_e32 v151, v151
	v_exp_f32_e32 v154, v154
	v_exp_f32_e32 v155, v155
	v_pk_add_f32 v[4:5], v[4:5], 1.0 op_sel_hi:[1,0]
	v_exp_f32_e32 v158, v158
	v_exp_f32_e32 v159, v159
	v_pk_add_f32 v[154:155], v[154:155], 1.0 op_sel_hi:[1,0]
	v_rcp_f32_e32 v4, v4
	v_rcp_f32_e32 v5, v5
	v_rcp_f32_e32 v154, v154
	v_rcp_f32_e32 v155, v155
	v_pk_add_f32 v[158:159], v[158:159], 1.0 op_sel_hi:[1,0]
	v_pk_add_f32 v[150:151], v[150:151], 1.0 op_sel_hi:[1,0]
	v_pk_add_f32 v[230:231], v[230:231], 1.0 op_sel_hi:[1,0]
	v_pk_mul_f32 v[4:5], v[150:151], v[4:5]
	v_pk_mul_f32 v[150:151], v[158:159], v[154:155]
	v_cvt_pk_f32_fp8_e32 v[154:155], v153
	v_cvt_pk_f32_fp8_sdwa v[152:153], v153 src0_sel:WORD_1
	v_pk_mul_f32 v[100:101], v[100:101], v[150:151]
	v_cvt_pk_f32_fp8_e32 v[150:151], v157
	v_pk_mul_f32 v[98:99], v[98:99], v[4:5]
	v_exp_f32_e32 v4, v154
	v_exp_f32_e32 v5, v155
	v_cvt_pk_f32_fp8_sdwa v[154:155], v157 src0_sel:WORD_1
	v_exp_f32_e32 v152, v152
	v_exp_f32_e32 v153, v153
	v_exp_f32_e32 v150, v150
	v_exp_f32_e32 v151, v151
	v_pk_add_f32 v[4:5], v[4:5], 1.0 op_sel_hi:[1,0]
	v_exp_f32_e32 v154, v154
	v_exp_f32_e32 v155, v155
	v_pk_add_f32 v[152:153], v[152:153], 1.0 op_sel_hi:[1,0]
	v_rcp_f32_e32 v4, v4
	v_rcp_f32_e32 v5, v5
	v_rcp_f32_e32 v152, v152
	v_rcp_f32_e32 v153, v153
	v_pk_add_f32 v[154:155], v[154:155], 1.0 op_sel_hi:[1,0]
	v_pk_add_f32 v[150:151], v[150:151], 1.0 op_sel_hi:[1,0]
	v_pk_add_f32 v[232:233], v[232:233], 1.0 op_sel_hi:[1,0]
	v_pk_mul_f32 v[4:5], v[150:151], v[4:5]
	v_pk_mul_f32 v[150:151], v[154:155], v[152:153]
	v_cvt_pk_f32_fp8_e32 v[152:153], v142
	v_pk_mul_f32 v[106:107], v[106:107], v[4:5]
	v_pk_mul_f32 v[108:109], v[108:109], v[150:151]
	s_waitcnt vmcnt(1)
	v_cvt_pk_f32_fp8_e32 v[150:151], v146
	v_exp_f32_e32 v4, v152
	v_exp_f32_e32 v5, v153
	v_cvt_pk_f32_fp8_sdwa v[152:153], v142 src0_sel:WORD_1
	v_cvt_pk_f32_fp8_sdwa v[154:155], v146 src0_sel:WORD_1
	v_exp_f32_e32 v150, v150
	v_exp_f32_e32 v151, v151
	v_exp_f32_e32 v152, v152
	v_exp_f32_e32 v153, v153
	v_pk_add_f32 v[4:5], v[4:5], 1.0 op_sel_hi:[1,0]
	v_exp_f32_e32 v154, v154
	v_exp_f32_e32 v155, v155
	v_pk_add_f32 v[152:153], v[152:153], 1.0 op_sel_hi:[1,0]
	v_rcp_f32_e32 v4, v4
	v_rcp_f32_e32 v5, v5
	v_rcp_f32_e32 v152, v152
	v_rcp_f32_e32 v153, v153
	v_pk_add_f32 v[154:155], v[154:155], 1.0 op_sel_hi:[1,0]
	v_pk_add_f32 v[150:151], v[150:151], 1.0 op_sel_hi:[1,0]
	v_pk_mul_f32 v[220:221], v[230:231], v[220:221]
	v_pk_mul_f32 v[4:5], v[150:151], v[4:5]
	v_pk_mul_f32 v[150:151], v[154:155], v[152:153]
	v_cvt_pk_f32_fp8_e32 v[152:153], v143
	v_cvt_pk_f32_fp8_sdwa v[142:143], v143 src0_sel:WORD_1
	v_pk_mul_f32 v[20:21], v[20:21], v[150:151]
	v_cvt_pk_f32_fp8_e32 v[150:151], v147
	v_cvt_pk_f32_fp8_sdwa v[146:147], v147 src0_sel:WORD_1
	v_exp_f32_e32 v142, v142
	v_exp_f32_e32 v143, v143
	v_pk_mul_f32 v[18:19], v[18:19], v[4:5]
	v_exp_f32_e32 v4, v152
	v_exp_f32_e32 v5, v153
	v_exp_f32_e32 v146, v146
	v_exp_f32_e32 v147, v147
	v_pk_add_f32 v[142:143], v[142:143], 1.0 op_sel_hi:[1,0]
	v_exp_f32_e32 v150, v150
	v_rcp_f32_e32 v142, v142
	v_rcp_f32_e32 v143, v143
	v_exp_f32_e32 v151, v151
	v_pk_add_f32 v[4:5], v[4:5], 1.0 op_sel_hi:[1,0]
	v_pk_add_f32 v[146:147], v[146:147], 1.0 op_sel_hi:[1,0]
	v_rcp_f32_e32 v4, v4
	v_rcp_f32_e32 v5, v5
	v_pk_mul_f32 v[142:143], v[146:147], v[142:143]
	v_cvt_pk_f32_fp8_e32 v[146:147], v144
	v_pk_add_f32 v[150:151], v[150:151], 1.0 op_sel_hi:[1,0]
	v_pk_mul_f32 v[16:17], v[16:17], v[142:143]
	v_pk_mul_f32 v[4:5], v[150:151], v[4:5]
	v_cvt_pk_f32_fp8_e32 v[142:143], v148
	v_pk_mul_f32 v[14:15], v[14:15], v[4:5]
	v_exp_f32_e32 v4, v146
	v_exp_f32_e32 v5, v147
	v_cvt_pk_f32_fp8_sdwa v[146:147], v144 src0_sel:WORD_1
	v_cvt_pk_f32_fp8_sdwa v[150:151], v148 src0_sel:WORD_1
	v_exp_f32_e32 v142, v142
	v_exp_f32_e32 v143, v143
	v_exp_f32_e32 v146, v146
	v_exp_f32_e32 v147, v147
	v_pk_add_f32 v[4:5], v[4:5], 1.0 op_sel_hi:[1,0]
	v_exp_f32_e32 v150, v150
	v_exp_f32_e32 v151, v151
	v_pk_add_f32 v[146:147], v[146:147], 1.0 op_sel_hi:[1,0]
	v_rcp_f32_e32 v4, v4
	v_rcp_f32_e32 v5, v5
	v_rcp_f32_e32 v146, v146
	v_rcp_f32_e32 v147, v147
	v_pk_add_f32 v[150:151], v[150:151], 1.0 op_sel_hi:[1,0]
	v_pk_add_f32 v[142:143], v[142:143], 1.0 op_sel_hi:[1,0]
	v_pk_mul_f32 v[222:223], v[232:233], v[222:223]
	v_pk_mul_f32 v[4:5], v[142:143], v[4:5]
	v_pk_mul_f32 v[142:143], v[150:151], v[146:147]
	v_cvt_pk_f32_fp8_e32 v[146:147], v145
	v_cvt_pk_f32_fp8_sdwa v[144:145], v145 src0_sel:WORD_1
	v_pk_mul_f32 v[120:121], v[120:121], v[142:143]
	v_cvt_pk_f32_fp8_e32 v[142:143], v149
	v_pk_mul_f32 v[118:119], v[118:119], v[4:5]
	v_exp_f32_e32 v4, v146
	v_exp_f32_e32 v5, v147
	v_cvt_pk_f32_fp8_sdwa v[146:147], v149 src0_sel:WORD_1
	v_exp_f32_e32 v144, v144
	v_exp_f32_e32 v145, v145
	v_exp_f32_e32 v142, v142
	v_exp_f32_e32 v143, v143
	v_pk_add_f32 v[4:5], v[4:5], 1.0 op_sel_hi:[1,0]
	v_exp_f32_e32 v146, v146
	v_exp_f32_e32 v147, v147
	v_pk_add_f32 v[144:145], v[144:145], 1.0 op_sel_hi:[1,0]
	v_rcp_f32_e32 v4, v4
	v_rcp_f32_e32 v5, v5
	v_rcp_f32_e32 v144, v144
	v_rcp_f32_e32 v145, v145
	v_pk_add_f32 v[146:147], v[146:147], 1.0 op_sel_hi:[1,0]
	v_pk_add_f32 v[142:143], v[142:143], 1.0 op_sel_hi:[1,0]
	v_pk_mul_f32 v[116:117], v[116:117], v[220:221]
	v_pk_mul_f32 v[4:5], v[142:143], v[4:5]
	v_pk_mul_f32 v[142:143], v[146:147], v[144:145]
	v_cvt_pk_f32_fp8_e32 v[144:145], v134
	v_pk_mul_f32 v[122:123], v[122:123], v[4:5]
	v_pk_mul_f32 v[124:125], v[124:125], v[142:143]
	s_waitcnt vmcnt(0)
; __device__ __forceinline__ float frcp_(float x) { return __builtin_amdgcn_rcpf(x); }
;     template <bool HI> static __device__ __forceinline__ f32x2 e1p(unsigned w) { const auto x = __builtin_amdgcn_cvt_pk_f32_fp8((int)w, HI); f32x2 e; e.x = __builtin_amdgcn_exp2f(x[0]); e.y = __builtin_amdgcn_exp2f(x[1]); return e + 1.0f; }
;     static __device__ __forceinline__ f32x2 rcp2(f32x2 d) { f32x2 r; r.x = frcp_(d.x); r.y = frcp_(d.y); return r; }
	v_cvt_pk_f32_fp8_e32 v[142:143], v138
	v_exp_f32_e32 v4, v144
	v_exp_f32_e32 v5, v145
	v_cvt_pk_f32_fp8_sdwa v[144:145], v134 src0_sel:WORD_1
	v_cvt_pk_f32_fp8_sdwa v[146:147], v138 src0_sel:WORD_1
	v_exp_f32_e32 v142, v142
	v_exp_f32_e32 v143, v143
	v_exp_f32_e32 v144, v144
	v_exp_f32_e32 v145, v145
	v_pk_add_f32 v[4:5], v[4:5], 1.0 op_sel_hi:[1,0]
	v_exp_f32_e32 v146, v146
	v_exp_f32_e32 v147, v147
	v_pk_add_f32 v[144:145], v[144:145], 1.0 op_sel_hi:[1,0]
	v_rcp_f32_e32 v4, v4
	v_rcp_f32_e32 v5, v5
	v_rcp_f32_e32 v144, v144
	v_rcp_f32_e32 v145, v145
	v_pk_add_f32 v[146:147], v[146:147], 1.0 op_sel_hi:[1,0]
	v_pk_add_f32 v[142:143], v[142:143], 1.0 op_sel_hi:[1,0]
	v_pk_mul_f32 v[110:111], v[110:111], v[222:223]
	v_pk_mul_f32 v[4:5], v[142:143], v[4:5]
	v_pk_mul_f32 v[142:143], v[146:147], v[144:145]
	v_cvt_pk_f32_fp8_e32 v[144:145], v135
	v_cvt_pk_f32_fp8_sdwa v[134:135], v135 src0_sel:WORD_1
	v_pk_mul_f32 v[12:13], v[12:13], v[142:143]
	v_cvt_pk_f32_fp8_e32 v[142:143], v139
	v_cvt_pk_f32_fp8_sdwa v[138:139], v139 src0_sel:WORD_1
	v_exp_f32_e32 v134, v134
	v_exp_f32_e32 v135, v135
	v_pk_mul_f32 v[10:11], v[10:11], v[4:5]
	v_exp_f32_e32 v4, v144
	v_exp_f32_e32 v5, v145
	v_exp_f32_e32 v138, v138
	v_exp_f32_e32 v139, v139
	v_pk_add_f32 v[134:135], v[134:135], 1.0 op_sel_hi:[1,0]
	v_exp_f32_e32 v142, v142
	v_rcp_f32_e32 v134, v134
	v_rcp_f32_e32 v135, v135
	v_exp_f32_e32 v143, v143
	v_pk_add_f32 v[4:5], v[4:5], 1.0 op_sel_hi:[1,0]
	v_pk_add_f32 v[138:139], v[138:139], 1.0 op_sel_hi:[1,0]
	v_rcp_f32_e32 v4, v4
	v_rcp_f32_e32 v5, v5
	v_pk_mul_f32 v[134:135], v[138:139], v[134:135]
	v_cvt_pk_f32_fp8_e32 v[138:139], v136
	v_pk_add_f32 v[142:143], v[142:143], 1.0 op_sel_hi:[1,0]
	v_pk_mul_f32 v[8:9], v[8:9], v[134:135]
	v_pk_mul_f32 v[4:5], v[142:143], v[4:5]
	v_cvt_pk_f32_fp8_e32 v[134:135], v140
	v_pk_mul_f32 v[6:7], v[6:7], v[4:5]
	v_exp_f32_e32 v4, v138
	v_exp_f32_e32 v5, v139
	v_cvt_pk_f32_fp8_sdwa v[138:139], v136 src0_sel:WORD_1
	v_cvt_pk_f32_fp8_sdwa v[142:143], v140 src0_sel:WORD_1
	v_exp_f32_e32 v134, v134
	v_exp_f32_e32 v135, v135
	v_exp_f32_e32 v138, v138
	v_exp_f32_e32 v139, v139
	v_pk_add_f32 v[4:5], v[4:5], 1.0 op_sel_hi:[1,0]
	v_exp_f32_e32 v142, v142
	v_exp_f32_e32 v143, v143
	v_pk_add_f32 v[138:139], v[138:139], 1.0 op_sel_hi:[1,0]
	v_rcp_f32_e32 v4, v4
	v_rcp_f32_e32 v5, v5
	v_rcp_f32_e32 v138, v138
	v_rcp_f32_e32 v139, v139
	v_pk_add_f32 v[142:143], v[142:143], 1.0 op_sel_hi:[1,0]
	v_pk_add_f32 v[134:135], v[134:135], 1.0 op_sel_hi:[1,0]
	s_nop 0
	v_pk_mul_f32 v[4:5], v[134:135], v[4:5]
	v_pk_mul_f32 v[134:135], v[142:143], v[138:139]
	v_cvt_pk_f32_fp8_e32 v[138:139], v137
	v_cvt_pk_f32_fp8_sdwa v[136:137], v137 src0_sel:WORD_1
	v_pk_mul_f32 v[128:129], v[128:129], v[134:135]
	v_cvt_pk_f32_fp8_e32 v[134:135], v141
	v_pk_mul_f32 v[126:127], v[126:127], v[4:5]
	v_exp_f32_e32 v4, v138
	v_exp_f32_e32 v5, v139
	v_cvt_pk_f32_fp8_sdwa v[138:139], v141 src0_sel:WORD_1
	v_exp_f32_e32 v136, v136
	v_exp_f32_e32 v137, v137
	v_exp_f32_e32 v134, v134
	v_exp_f32_e32 v135, v135
	v_pk_add_f32 v[4:5], v[4:5], 1.0 op_sel_hi:[1,0]
	v_exp_f32_e32 v138, v138
	v_exp_f32_e32 v139, v139
	v_pk_add_f32 v[136:137], v[136:137], 1.0 op_sel_hi:[1,0]
	v_rcp_f32_e32 v4, v4
	v_rcp_f32_e32 v5, v5
	v_rcp_f32_e32 v136, v136
	v_rcp_f32_e32 v137, v137
	v_pk_add_f32 v[138:139], v[138:139], 1.0 op_sel_hi:[1,0]
	v_pk_add_f32 v[134:135], v[134:135], 1.0 op_sel_hi:[1,0]
	s_nop 0
	v_pk_mul_f32 v[4:5], v[134:135], v[4:5]
	v_pk_mul_f32 v[134:135], v[138:139], v[136:137]
	v_pk_mul_f32 v[130:131], v[130:131], v[4:5]
	v_pk_mul_f32 v[132:133], v[132:133], v[134:135]
	s_and_b64 vcc, exec, s[0:1]
	s_mov_b64 s[0:1], -1
	s_cbranch_vccnz .LBB0_646
